# queue-ticket atomics made asynchronous, Q-load waits removed from unit prologues, conversion-group weight loads issued at unit top for window/SWA units
# baseline (speedup 1.0000x reference)
.LBB0_420:
	s_setprio 0
	v_mov_b32_e32 v2, v0
	s_barrier
	s_nop 0
	v_cmp_eq_u32_e32 vcc, 0, v2
	s_and_saveexec_b64 s[2:3], vcc
	s_cbranch_execz .LBB0_426
	v_mov_b32_e32 v206, 1
	v_mov_b32_e32 v207, 1
	global_atomic_add v206, v3, v206, s[12:13] sc0
	global_atomic_add v207, v3, v207, s[10:11] sc0
	s_waitcnt vmcnt(0)
	v_mov_b32_e32 v6, v206
	v_min_u32_e32 v7, 0xc00, v207
	v_mov_b32_e32 v2, s73
	ds_write_b64 v2, v[6:7]

.LBB0_437:
	s_mul_i32 s4, s28, 0x3600
	s_mul_hi_i32 s5, s28, 0x3600
	s_add_u32 s30, s14, s4
	v_mov_b32_e32 v6, v151
	v_readfirstlane_b32 s29, v5
	s_addc_u32 s31, s15, s5
	s_mov_b32 m0, s29
	v_readfirstlane_b32 s29, v4
	global_load_lds_dwordx4 v6, s[30:31]
	v_mov_b32_e32 v6, v153
	s_mov_b32 m0, s29
	v_add_u32_e32 v7, 0x4000, v5
	s_add_u32 s4, s16, s4
	global_load_lds_dwordx4 v6, s[30:31]
	v_mov_b32_e32 v6, v155
	v_readfirstlane_b32 s29, v7
	v_add_u32_e32 v7, 0x6000, v5
	s_addc_u32 s5, s17, s5
	s_mov_b32 m0, s29
	v_readfirstlane_b32 s29, v7
	global_load_lds_dwordx4 v6, s[4:5]
	v_mov_b32_e32 v6, v157
	s_mov_b32 m0, s29
	s_add_i32 s27, s27, -1
	global_load_lds_dwordx4 v6, s[4:5]
	s_sub_i32 s28, s28, 64
	v_add_u32_e32 v4, 0x8000, v4
	v_add_u32_e32 v5, 0x8000, v5
	s_cmp_eq_u32 s27, 0
	s_cbranch_scc0 .LBB0_437
	s_ashr_i32 s4, s3, 2
	s_andn2_b32 s4, s4, 31
	s_and_b32 s5, s19, 1
	s_lshl_b32 s19, s22, 7
	v_and_b32_e32 v159, 31, v2
	s_add_i32 s19, s4, s19
	v_or_b32_e32 v4, s19, v159
	s_mov_b32 s3, s83
	v_ashrrev_i32_e32 v5, 31, v4
	v_lshl_add_u64 v[138:139], v[4:5], 0, s[2:3]
	v_mov_b64_e32 v[4:5], s[8:9]
	v_mad_u64_u32 v[4:5], s[2:3], v138, s70, v[4:5]
	v_mad_i32_i24 v5, v139, s70, v5
	s_lshl_b32 s2, s82, 1
	s_mov_b32 s3, s83
	v_bfe_u32 v12, v2, 5, 1
	v_lshl_add_u64 v[4:5], v[4:5], 0, s[2:3]
	s_lshl_b32 s2, s5, 7
	v_lshl_add_u64 v[4:5], v[4:5], 0, s[2:3]
	v_lshlrev_b32_e32 v144, 4, v12
	v_mov_b32_e32 v145, v3
	v_lshl_add_u64 v[4:5], v[4:5], 0, v[144:145]
	global_load_dwordx4 v[86:89], v[4:5], off offset:1536
	global_load_dwordx4 v[90:93], v[4:5], off offset:1568
	global_load_dword v143, v3, s[20:21]
	global_load_dwordx4 v[94:97], v[4:5], off offset:1600
	global_load_dwordx4 v[98:101], v[4:5], off offset:1632
	v_and_b32_e32 v13, 63, v2
	v_lshlrev_b32_e32 v15, 3, v2
	s_not_b32 s2, s23
	v_bfe_u32 v16, v2, 2, 2
	v_bfe_u32 v17, v2, 3, 3
	v_and_b32_e32 v160, 8, v15
	v_bfe_u32 v15, v13, 1, 1
	s_lshl_b32 s2, s2, 1
	v_lshlrev_b32_e32 v18, 6, v16
	v_and_or_b32 v16, v17, 4, v16
	v_and_or_b32 v15, v17, 2, v15
	v_ldexp_f32 v20, 1.0, s2
	v_lshlrev_b32_e32 v16, 8, v16
	v_lshl_or_b32 v15, v15, 4, v18
	s_movk_i32 s2, 0x2040
	v_lshlrev_b32_e32 v14, 7, v2
	v_lshlrev_b32_e32 v19, 2, v12
	v_bitop3_b32 v146, v15, s2, v16 bitop3:0x36
	s_movk_i32 s2, 0x2080
	v_and_b32_e32 v145, 0xf00, v14
	v_bfe_u32 v14, v13, 1, 4
	v_sub_u32_e32 v161, v159, v19
	v_sub_u32_e32 v17, v19, v159
	v_mul_f32_e32 v19, 0x43800000, v20
	v_and_b32_e32 v20, 0x7fff0000, v20
	v_bitop3_b32 v148, v15, s2, v16 bitop3:0x36
	s_movk_i32 s2, 0x20c0
	v_lshlrev_b32_e32 v140, 3, v12
	v_or_b32_e32 v21, v160, v12
	v_bitop3_b32 v12, v160, v14, v12 bitop3:0x36
	v_subrev_u32_e32 v163, s4, v17
	v_or_b32_sdwa v17, v19, v20 dst_sel:DWORD dst_unused:UNUSED_PAD src0_sel:WORD_1 src1_sel:DWORD
	v_bitop3_b32 v150, v15, s2, v16 bitop3:0x36
	s_movk_i32 s2, 0xc0
	v_cmp_gt_u32_e64 s[36:37], 32, v13
	v_lshlrev_b32_e32 v162, 4, v12
	v_bitop3_b32 v12, v21, v14, 2 bitop3:0x36
	v_bitop3_b32 v22, v21, v14, 4 bitop3:0x36
	v_bitop3_b32 v14, v21, v14, 6 bitop3:0x36
	v_or_b32_e32 v142, v15, v16
	v_bitop3_b32 v152, v15, 64, v16 bitop3:0x36
	v_bitop3_b32 v154, v15, s71, v16 bitop3:0x36
	v_bitop3_b32 v156, v15, s2, v16 bitop3:0x36
	v_cndmask_b32_e64 v102, 0, v17, s[36:37]
	v_mov_b32_e32 v16, v3
	v_mov_b32_e32 v17, v3
	v_mov_b32_e32 v2, v3
	v_mov_b32_e32 v4, v3
	v_mov_b32_e32 v5, v3
	v_mov_b32_e32 v6, v3
	v_mov_b32_e32 v7, v3
	v_mov_b32_e32 v8, v3
	v_mov_b32_e32 v9, v3
	v_mov_b32_e32 v10, v3
	v_mov_b32_e32 v11, v3
	v_lshlrev_b32_e32 v164, 4, v12
	v_lshlrev_b32_e32 v165, 4, v22
	v_lshlrev_b32_e32 v166, 4, v14
	v_mov_b32_e32 v12, v3
	v_mov_b32_e32 v13, v3
	v_mov_b32_e32 v14, v3
	v_mov_b32_e32 v15, v3
	v_mov_b64_e32 v[68:69], v[16:17]
	v_mov_b64_e32 v[52:53], v[16:17]
	v_mov_b64_e32 v[36:37], v[16:17]
	v_mov_b64_e32 v[66:67], v[14:15]
	v_mov_b64_e32 v[64:65], v[12:13]
	v_mov_b64_e32 v[62:63], v[10:11]
	v_mov_b64_e32 v[60:61], v[8:9]
	v_mov_b64_e32 v[58:59], v[6:7]
	v_mov_b64_e32 v[56:57], v[4:5]
	v_mov_b64_e32 v[54:55], v[2:3]
	v_mov_b64_e32 v[50:51], v[14:15]
	v_mov_b64_e32 v[48:49], v[12:13]
	v_mov_b64_e32 v[46:47], v[10:11]
	v_mov_b64_e32 v[44:45], v[8:9]
	v_mov_b64_e32 v[42:43], v[6:7]
	v_mov_b64_e32 v[40:41], v[4:5]
	v_mov_b64_e32 v[38:39], v[2:3]
	v_mov_b64_e32 v[34:35], v[14:15]
	v_mov_b64_e32 v[32:33], v[12:13]
	v_mov_b64_e32 v[30:31], v[10:11]
	v_mov_b64_e32 v[28:29], v[8:9]
	v_mov_b64_e32 v[26:27], v[6:7]
	v_mov_b64_e32 v[24:25], v[4:5]
	v_mov_b64_e32 v[22:23], v[2:3]
	v_mov_b64_e32 v[20:21], v[16:17]
	s_mov_b32 s22, 3
	v_mov_b32_e32 v141, v3
	s_mov_b32 s23, 0
	v_mov_b32_e32 v103, v3
	v_mov_b32_e32 v104, v3
	v_mov_b32_e32 v105, v3
	s_sub_i32 s26, 0, s26
	s_lshl_b32 s27, s5, 13
	s_or_b32 s28, s19, 31
	v_mov_b32_e32 v167, 0
	v_mov_b32_e32 v168, 0xf149f2ca
	s_mov_b32 s29, s4
	s_mov_b32 s30, 0
	s_mov_b32 s33, s18
	v_mov_b64_e32 v[18:19], v[14:15]
	v_mov_b64_e32 v[16:17], v[12:13]
	v_mov_b64_e32 v[14:15], v[10:11]
	v_mov_b64_e32 v[12:13], v[8:9]
	v_mov_b64_e32 v[10:11], v[6:7]
	v_mov_b64_e32 v[8:9], v[4:5]
	v_mov_b64_e32 v[6:7], v[2:3]
	s_waitcnt vmcnt(0)
	.p2align 8
	s_add_i32 s31, s33, -1
	s_cmp_lt_i32 s31, 2
	s_mov_b64 s[2:3], -1
	s_cbranch_scc0 .LBB0_445
	s_branch .LBB0_440

.LBB0_496:
	v_mov_b32_e32 v2, v0
	v_mov_b32_e32 v90, 0
	v_cmp_eq_u32_e32 vcc, 0, v2
	v_mov_b32_e32 v91, 0xc00
	s_and_saveexec_b64 s[2:3], vcc
	s_cbranch_execz .LBB0_502
	v_mov_b32_e32 v122, 1
	v_mov_b32_e32 v123, 1
	global_atomic_add v122, v3, v122, s[4:5] sc0
	global_atomic_add v123, v3, v123, s[10:11] sc0
.LBB0_502:
	s_or_b64 exec, exec, s[2:3]
	s_cmpk_gt_i32 s16, 0xbff
	s_cbranch_scc1 .Lpf_win_skip
	s_mul_hi_i32 s84, s16, 0x2aaaaaab
	s_lshr_b32 s84, s84, 4
	s_mul_i32 s85, s84, 0xffffffa0
	s_add_i32 s85, s85, s16
	v_readlane_b32 s87, v254, 7
	v_readlane_b32 s88, v253, 1
	v_readlane_b32 s89, v253, 2
	s_lshl_b32 s86, s16, 7
	s_and_b32 s86, s86, 0x380
	v_ashrrev_i32_e32 v238, 2, v0
	v_and_b32_e32 v238, -4, v238
	v_add_u32_e32 v238, s86, v238
	v_lshlrev_b32_e32 v240, 4, v0
	v_and_b32_e32 v240, 0xf0, v240
	s_lshl_b32 s87, s87, 5
	s_add_i32 s92, s84, s87
	s_mov_b32 s93, 0
	s_cmp_gt_i32 s85, 63
	s_cbranch_scc1 .Lpf_win_w2
	s_load_dwordx2 s[90:91], s[88:89], 0xa0
	s_lshl_b64 s[92:93], s[92:93], 23
	v_lshlrev_b32_e32 v238, 13, v238
	s_lshl_b32 s86, s85, 4
	s_and_b32 s86, s86, 0xffffff80
	s_lshl_b32 s86, s86, 2
	v_add3_u32 v238, v238, v240, s86
	v_mov_b32_e32 v239, 0
	s_waitcnt lgkmcnt(0)
	s_add_u32 s90, s90, s92
	s_addc_u32 s91, s91, s93
	v_lshl_add_u64 v[238:239], s[90:91], 0, v[238:239]
	s_mov_b64 s[94:95], 0x2000
	v_lshl_add_u64 v[240:241], v[238:239], 0, s[94:95]
	global_load_dwordx4 v[126:129], v[240:241], off nt
	s_mov_b64 s[94:95], 0x4000
	v_lshl_add_u64 v[242:243], v[238:239], 0, s[94:95]
	global_load_dwordx4 v[130:133], v[242:243], off nt
	global_load_dwordx4 v[134:137], v[238:239], off nt
	global_load_dwordx4 v[138:141], v[238:239], off offset:256 nt
	s_mov_b64 s[94:95], 0x6000
	v_lshl_add_u64 v[240:241], v[238:239], 0, s[94:95]
	global_load_dwordx4 v[142:145], v[240:241], off nt
	s_mov_b64 s[94:95], 0x2000
	v_lshl_add_u64 v[242:243], v[238:239], 0, s[94:95]
	global_load_dwordx4 v[146:149], v[242:243], off offset:256 nt
	s_mov_b64 s[94:95], 0x4000
	v_lshl_add_u64 v[240:241], v[238:239], 0, s[94:95]
	global_load_dwordx4 v[168:171], v[240:241], off offset:256 nt
	s_mov_b64 s[94:95], 0x6000
	v_lshl_add_u64 v[242:243], v[238:239], 0, s[94:95]
	global_load_dwordx4 v[172:175], v[242:243], off offset:256 nt
	s_mov_b64 s[94:95], 0x1000
	v_lshl_add_u64 v[240:241], v[238:239], 0, s[94:95]
	global_load_dwordx4 v[176:179], v[240:241], off nt
	s_mov_b64 s[94:95], 0x3000
	v_lshl_add_u64 v[242:243], v[238:239], 0, s[94:95]
	global_load_dwordx4 v[206:209], v[242:243], off nt
	s_mov_b64 s[94:95], 0x5000
	v_lshl_add_u64 v[240:241], v[238:239], 0, s[94:95]
	global_load_dwordx4 v[210:213], v[240:241], off nt
	s_mov_b64 s[94:95], 0x7000
	v_lshl_add_u64 v[242:243], v[238:239], 0, s[94:95]
	global_load_dwordx4 v[214:217], v[242:243], off nt
	s_mov_b64 s[94:95], 0x1000
	v_lshl_add_u64 v[240:241], v[238:239], 0, s[94:95]
	global_load_dwordx4 v[222:225], v[240:241], off offset:256 nt
	s_mov_b64 s[94:95], 0x3000
	v_lshl_add_u64 v[242:243], v[238:239], 0, s[94:95]
	global_load_dwordx4 v[226:229], v[242:243], off offset:256 nt
	s_mov_b64 s[94:95], 0x5000
	v_lshl_add_u64 v[240:241], v[238:239], 0, s[94:95]
	global_load_dwordx4 v[230:233], v[240:241], off offset:256 nt
	s_mov_b64 s[94:95], 0x7000
	v_lshl_add_u64 v[242:243], v[238:239], 0, s[94:95]
	global_load_dwordx4 v[234:237], v[242:243], off offset:256 nt
	s_branch .Lpf_win_skip
.Lpf_win_w2:
	s_load_dwordx2 s[90:91], s[88:89], 0xb0
	s_lshl_b64 s[92:93], s[92:93], 22
	v_lshlrev_b32_e32 v238, 12, v238
	s_lshl_b32 s86, s85, 5
	s_and_b32 s86, s86, 0xffffff00
	s_add_i32 s86, s86, 0xfffff800
	s_lshl_b32 s86, s86, 2
	v_add3_u32 v238, v238, v240, s86
	v_mov_b32_e32 v239, 0
	s_waitcnt lgkmcnt(0)
	s_add_u32 s90, s90, s92
	s_addc_u32 s91, s91, s93
	v_lshl_add_u64 v[238:239], s[90:91], 0, v[238:239]
	s_mov_b64 s[94:95], 0x1000
	v_lshl_add_u64 v[240:241], v[238:239], 0, s[94:95]
	global_load_dwordx4 v[126:129], v[240:241], off nt
	s_mov_b64 s[94:95], 0x2000
	v_lshl_add_u64 v[242:243], v[238:239], 0, s[94:95]
	global_load_dwordx4 v[130:133], v[242:243], off nt
	global_load_dwordx4 v[134:137], v[238:239], off nt
	global_load_dwordx4 v[138:141], v[238:239], off offset:256 nt
	s_mov_b64 s[94:95], 0x3000
	v_lshl_add_u64 v[240:241], v[238:239], 0, s[94:95]
	global_load_dwordx4 v[142:145], v[240:241], off nt
	s_mov_b64 s[94:95], 0x1000
	v_lshl_add_u64 v[242:243], v[238:239], 0, s[94:95]
	global_load_dwordx4 v[146:149], v[242:243], off offset:256 nt
	s_mov_b64 s[94:95], 0x2000
	v_lshl_add_u64 v[240:241], v[238:239], 0, s[94:95]
	global_load_dwordx4 v[168:171], v[240:241], off offset:256 nt
	s_mov_b64 s[94:95], 0x3000
	v_lshl_add_u64 v[242:243], v[238:239], 0, s[94:95]
	global_load_dwordx4 v[172:175], v[242:243], off offset:256 nt
	global_load_dwordx4 v[176:179], v[238:239], off offset:512 nt
	s_mov_b64 s[94:95], 0x1000
	v_lshl_add_u64 v[240:241], v[238:239], 0, s[94:95]
	global_load_dwordx4 v[206:209], v[240:241], off offset:512 nt
	s_mov_b64 s[94:95], 0x2000
	v_lshl_add_u64 v[242:243], v[238:239], 0, s[94:95]
	global_load_dwordx4 v[210:213], v[242:243], off offset:512 nt
	s_mov_b64 s[94:95], 0x3000
	v_lshl_add_u64 v[240:241], v[238:239], 0, s[94:95]
	global_load_dwordx4 v[214:217], v[240:241], off offset:512 nt
	global_load_dwordx4 v[222:225], v[238:239], off offset:768 nt
	s_mov_b64 s[94:95], 0x1000
	v_lshl_add_u64 v[242:243], v[238:239], 0, s[94:95]
	global_load_dwordx4 v[226:229], v[242:243], off offset:768 nt
	s_mov_b64 s[94:95], 0x2000
	v_lshl_add_u64 v[240:241], v[238:239], 0, s[94:95]
	global_load_dwordx4 v[230:233], v[240:241], off offset:768 nt
	s_mov_b64 s[94:95], 0x3000
	v_lshl_add_u64 v[242:243], v[238:239], 0, s[94:95]
	global_load_dwordx4 v[234:237], v[242:243], off offset:768 nt
.Lpf_win_skip:
	v_mov_b32_e32 v4, v0
	s_nop 0
	v_readfirstlane_b32 s19, v4
	s_ashr_i32 s18, s19, 6
	s_cmp_lt_i32 s18, 4
	s_cbranch_scc1 .LBB0_504
	s_setprio 1

.LBB0_507:
	s_ashr_i32 s19, s19, 3
	s_andn2_b32 s19, s19, 31
	v_and_b32_e32 v99, 31, v4
	s_add_i32 s20, s19, s20
	v_or_b32_e32 v6, s20, v99
	v_ashrrev_i32_e32 v7, 31, v6
	s_and_b32 s18, s18, 3
	s_lshl_b32 s21, s21, 2
	v_lshl_add_u64 v[92:93], v[6:7], 0, s[82:83]
	v_mov_b64_e32 v[6:7], s[8:9]
	s_or_b32 s18, s18, s21
	v_mad_u64_u32 v[6:7], s[22:23], v92, s70, v[6:7]
	v_bfe_u32 v98, v4, 5, 1
	v_mad_i32_i24 v7, v93, s70, v7
	s_lshl_b32 s82, s18, 7
	v_lshl_add_u64 v[6:7], v[6:7], 0, s[82:83]
	v_lshlrev_b32_e32 v2, 4, v98
	v_lshl_add_u64 v[6:7], v[6:7], 0, v[2:3]
	s_mov_b64 s[22:23], 0x1200
	s_movk_i32 s21, 0x1000
	v_lshl_add_u64 v[124:125], v[6:7], 0, s[22:23]
	v_add_co_u32_e32 v6, vcc, s21, v6
	s_cmp_lt_i32 s17, 0
	s_nop 0
	v_addc_co_u32_e32 v7, vcc, 0, v7, vcc
	global_load_dwordx4 v[66:69], v[124:125], off offset:32
	global_load_dwordx4 v[70:73], v[124:125], off offset:64
	global_load_dwordx4 v[74:77], v[6:7], off offset:512
	global_load_dwordx4 v[78:81], v[124:125], off offset:96
	s_waitcnt vmcnt(0)
	v_mov_b32_e32 v90, v122
	v_min_u32_e32 v91, 0xc00, v123
	.p2align 8
	s_cbranch_scc1 .LBB0_532
	s_add_i32 s22, s18, 1
	v_and_b32_e32 v2, 63, v4
	v_cvt_f32_ubyte0_e32 v4, s22
	s_mov_b32 s22, 0x42fc0000
	v_cmp_lt_f32_e32 vcc, s22, v4
	v_mov_b32_e32 v5, 0x42800000
	s_and_b64 s[24:25], vcc, exec
	v_cndmask_b32_e32 v5, 0, v5, vcc
	v_sub_f32_e32 v4, v5, v4
	v_exp_f32_e32 v4, v4
	s_cselect_b32 s23, 0xffffffc0, 0
	v_bfe_u32 v6, v2, 1, 4
	v_cmp_gt_u32_e64 s[36:37], 32, v2
	v_ldexp_f32 v4, v4, s23
	v_mul_f32_e32 v5, 0x43800000, v4
	v_and_b32_e32 v4, 0x7fff0000, v4
	v_or_b32_sdwa v4, v5, v4 dst_sel:DWORD dst_unused:UNUSED_PAD src0_sel:WORD_1 src1_sel:DWORD
	v_lshlrev_b32_e32 v5, 7, v2
	v_and_b32_e32 v100, 0xf00, v5
	v_lshlrev_b32_e32 v5, 3, v2
	v_and_b32_e32 v94, 8, v5
	v_or_b32_e32 v5, v94, v98
	v_bitop3_b32 v7, v94, v6, v98 bitop3:0x36
	v_lshlrev_b32_e32 v101, 4, v7
	v_bitop3_b32 v7, v5, v6, 2 bitop3:0x36
	v_lshlrev_b32_e32 v102, 4, v7
	v_bitop3_b32 v7, v5, v6, 4 bitop3:0x36
	v_bitop3_b32 v5, v5, v6, 6 bitop3:0x36
	v_lshlrev_b32_e32 v104, 4, v5
	v_lshrrev_b32_e32 v5, 2, v2
	v_lshlrev_b32_e32 v103, 4, v7
	v_and_b32_e32 v5, 2, v5
	v_lshrrev_b32_e32 v6, 3, v2
	v_bfe_u32 v7, v2, 1, 1
	v_cndmask_b32_e64 v82, 0, v4, s[36:37]
	v_lshrrev_b32_e32 v4, 1, v2
	v_and_or_b32 v5, v6, 4, v5
	v_and_or_b32 v6, v6, 2, v7
	v_bfe_u32 v2, v2, 3, 1
	v_and_or_b32 v2, v4, 2, v2
	v_lshlrev_b32_e32 v4, 4, v6
	v_lshl_or_b32 v2, v2, 6, v4
	v_lshlrev_b32_e32 v4, 2, v98
	v_lshlrev_b32_e32 v5, 7, v5
	v_or_b32_e32 v105, v2, v5
	v_bitop3_b32 v106, v2, 64, v5 bitop3:0x36
	v_sub_u32_e32 v2, v4, v99
	v_mov_b32_e32 v16, v3
	v_mov_b32_e32 v17, v3
	s_add_i32 s26, s2, s3
	s_sub_i32 s27, 0, s2
	s_lshl_b32 s2, s2, 6
	v_sub_u32_e32 v108, v99, v4
	v_subrev_u32_e32 v109, s19, v2
	v_mov_b32_e32 v2, v3
	v_mov_b32_e32 v4, v3
	v_mov_b32_e32 v5, v3
	v_mov_b32_e32 v6, v3
	v_mov_b32_e32 v7, v3
	v_mov_b32_e32 v8, v3
	v_mov_b32_e32 v9, v3
	v_mov_b32_e32 v10, v3
	v_mov_b32_e32 v11, v3
	v_mov_b32_e32 v12, v3
	v_mov_b32_e32 v13, v3
	v_mov_b32_e32 v14, v3
	v_mov_b32_e32 v15, v3
	v_mov_b64_e32 v[32:33], v[16:17]
	v_mov_b64_e32 v[48:49], v[16:17]
	s_mov_b32 s21, 32
	s_mov_b32 s22, 0
	v_mov_b32_e32 v83, v3
	v_mov_b32_e32 v84, v3
	v_mov_b32_e32 v85, v3
	s_or_b32 s23, s20, 31
	s_add_i32 s24, s20, 0xfffffe01
	s_mov_b32 s25, 3
	s_sub_i32 s26, 0, s26
	s_sub_i32 s28, s27, s3
	s_sub_i32 s29, 0, s2
	v_mov_b32_e32 v110, 0xf149f2ca
	v_mov_b32_e32 v107, 0
	s_mov_b32 s30, 0
	v_mov_b64_e32 v[30:31], v[14:15]
	v_mov_b64_e32 v[28:29], v[12:13]
	v_mov_b64_e32 v[26:27], v[10:11]
	v_mov_b64_e32 v[24:25], v[8:9]
	v_mov_b64_e32 v[22:23], v[6:7]
	v_mov_b64_e32 v[20:21], v[4:5]
	v_mov_b64_e32 v[18:19], v[2:3]
	v_mov_b64_e32 v[46:47], v[14:15]
	v_mov_b64_e32 v[44:45], v[12:13]
	v_mov_b64_e32 v[42:43], v[10:11]
	v_mov_b64_e32 v[40:41], v[8:9]
	v_mov_b64_e32 v[38:39], v[6:7]
	v_mov_b64_e32 v[36:37], v[4:5]
	v_mov_b64_e32 v[34:35], v[2:3]
	s_branch .LBB0_511

.LBB0_539:
	v_lshlrev_b32_e32 v36, 4, v38
	v_and_b32_e32 v2, 0xf0, v36
	v_lshl_add_u64 v[28:29], v[4:5], 0, v[2:3]
	v_lshl_add_u64 v[4:5], v[28:29], 0, s[42:43]
	v_lshl_add_u64 v[6:7], v[28:29], 0, s[40:41]
	v_mov_b32_e32 v40, v126
	v_mov_b32_e32 v41, v127
	v_mov_b32_e32 v42, v128
	v_mov_b32_e32 v43, v129
	v_mov_b32_e32 v44, v130
	v_mov_b32_e32 v45, v131
	v_mov_b32_e32 v46, v132
	v_mov_b32_e32 v47, v133
	v_lshl_add_u64 v[4:5], v[28:29], 0, s[38:39]
	v_mov_b32_e32 v84, v134
	v_mov_b32_e32 v85, v135
	v_mov_b32_e32 v86, v136
	v_mov_b32_e32 v87, v137
	v_mov_b32_e32 v66, v138
	v_mov_b32_e32 v67, v139
	v_mov_b32_e32 v68, v140
	v_mov_b32_e32 v69, v141
	v_lshl_add_u64 v[6:7], v[28:29], 0, s[36:37]
	v_mov_b32_e32 v76, v142
	v_mov_b32_e32 v77, v143
	v_mov_b32_e32 v78, v144
	v_mov_b32_e32 v79, v145
	v_mov_b32_e32 v70, v146
	v_mov_b32_e32 v71, v147
	v_mov_b32_e32 v72, v148
	v_mov_b32_e32 v73, v149
	v_lshl_add_u64 v[4:5], v[28:29], 0, s[34:35]
	v_lshl_add_u64 v[6:7], v[28:29], 0, s[30:31]
	v_mov_b32_e32 v60, v168
	v_mov_b32_e32 v61, v169
	v_mov_b32_e32 v62, v170
	v_mov_b32_e32 v63, v171
	v_mov_b32_e32 v92, v172
	v_mov_b32_e32 v93, v173
	v_mov_b32_e32 v94, v174
	v_mov_b32_e32 v95, v175
	v_lshl_add_u64 v[4:5], v[28:29], 0, s[28:29]
	v_lshl_add_u64 v[8:9], v[28:29], 0, s[26:27]
	v_lshl_add_u64 v[12:13], v[28:29], 0, s[24:25]
	v_lshl_add_u64 v[16:17], v[28:29], 0, s[22:23]
	v_lshl_add_u64 v[20:21], v[28:29], 0, s[20:21]
	v_lshl_add_u64 v[24:25], v[28:29], 0, s[18:19]
	v_lshl_add_u64 v[30:31], v[28:29], 0, s[16:17]
	v_lshl_add_u64 v[32:33], v[28:29], 0, s[14:15]
	v_mov_b32_e32 v4, v176
	v_mov_b32_e32 v5, v177
	v_mov_b32_e32 v6, v178
	v_mov_b32_e32 v7, v179
	v_mov_b32_e32 v8, v206
	v_mov_b32_e32 v9, v207
	v_mov_b32_e32 v10, v208
	v_mov_b32_e32 v11, v209
	v_mov_b32_e32 v12, v210
	v_mov_b32_e32 v13, v211
	v_mov_b32_e32 v14, v212
	v_mov_b32_e32 v15, v213
	v_mov_b32_e32 v16, v214
	v_mov_b32_e32 v17, v215
	v_mov_b32_e32 v18, v216
	v_mov_b32_e32 v19, v217
	v_mov_b32_e32 v20, v222
	v_mov_b32_e32 v21, v223
	v_mov_b32_e32 v22, v224
	v_mov_b32_e32 v23, v225
	v_mov_b32_e32 v24, v226
	v_mov_b32_e32 v25, v227
	v_mov_b32_e32 v26, v228
	v_mov_b32_e32 v27, v229
	v_mov_b32_e32 v28, v230
	v_mov_b32_e32 v29, v231
	v_mov_b32_e32 v30, v232
	v_mov_b32_e32 v31, v233
	v_mov_b32_e32 v32, v234
	v_mov_b32_e32 v33, v235
	v_mov_b32_e32 v34, v236
	v_mov_b32_e32 v35, v237
	v_ashrrev_i32_e32 v39, 6, v38
	v_lshlrev_b32_e32 v37, 9, v38
	v_bitop3_b32 v39, v39, v38, 7 bitop3:0x78
	v_lshrrev_b32_e32 v2, 2, v38
	v_and_b32_e32 v37, 0x1e00, v37
	v_lshlrev_b32_e32 v39, 4, v39
	v_add3_u32 v39, 0, v37, v39
	v_and_b32_e32 v48, 12, v2
	v_ashrrev_i32_e32 v37, 3, v38
	v_lshrrev_b32_e32 v49, 5, v38
	v_add_u32_e32 v48, v39, v48
	v_and_b32_e32 v2, 0x70, v36
	v_add_u32_e32 v36, s44, v37
	s_mov_b64 s[14:15], -1
	s_and_b64 vcc, exec, s[2:3]
	v_lshlrev_b32_e32 v37, 7, v37
	v_xor_b32_e32 v82, v49, v38
	v_mul_f32_e32 v49, 0x42000000, v95
	v_mul_f32_e32 v50, 0x42000000, v63
	v_mul_f32_e32 v52, 0x42000000, v73
	v_mul_f32_e32 v54, 0x42000000, v69
	v_mul_f32_e32 v51, 0x42000000, v94
	v_mul_f32_e32 v53, 0x42000000, v62
	v_mul_f32_e32 v57, 0x42000000, v72
	v_mul_f32_e32 v58, 0x42000000, v68
	v_mul_f32_e32 v55, 0x42000000, v93
	v_mul_f32_e32 v56, 0x42000000, v61
	v_mul_f32_e32 v61, 0x42000000, v71
	v_mul_f32_e32 v62, 0x42000000, v67
	v_mul_f32_e32 v59, 0x42000000, v92
	v_mul_f32_e32 v60, 0x42000000, v60
	v_mul_f32_e32 v64, 0x42000000, v70
	v_mul_f32_e32 v65, 0x42000000, v66
	v_mul_f32_e32 v66, 0x42000000, v79
	v_mul_f32_e32 v67, 0x42000000, v47
	v_mul_f32_e32 v69, 0x42000000, v43
	v_mul_f32_e32 v71, 0x42000000, v87
	v_mul_f32_e32 v68, 0x42000000, v78
	v_mul_f32_e32 v70, 0x42000000, v46
	v_mul_f32_e32 v74, 0x42000000, v42
	v_mul_f32_e32 v75, 0x42000000, v86
	v_mul_f32_e32 v72, 0x42000000, v77
	v_mul_f32_e32 v73, 0x42000000, v45
	v_mul_f32_e32 v78, 0x42000000, v41
	v_mul_f32_e32 v79, 0x42000000, v85
	v_mul_f32_e32 v76, 0x42000000, v76
	v_mul_f32_e32 v77, 0x42000000, v44
	v_mul_f32_e32 v80, 0x42000000, v40
	v_mul_f32_e32 v81, 0x42000000, v84
	v_add_u32_e32 v63, 0x2000, v48
	v_add_u32_e32 v47, 0x4000, v48
	v_add_u32_e32 v46, 0x6000, v48
	s_barrier
	s_cbranch_vccz .LBB0_541
	v_mov_b32_e32 v118, v3
	v_mov_b32_e32 v119, v3
	v_cvt_pk_fp8_f32 v118, v81, v80
	v_cvt_pk_fp8_f32 v119, v79, v78
	v_mul_f32_e32 v116, 0x42000000, v8
	v_mul_f32_e32 v117, 0x42000000, v4
	v_cvt_pk_fp8_f32 v118, v77, v76 op_sel:[0,0,1]
	v_cvt_pk_fp8_f32 v119, v73, v72 op_sel:[0,0,1]
	v_mul_f32_e32 v114, 0x42000000, v16
	v_mul_f32_e32 v115, 0x42000000, v12
	v_mul_f32_e32 v112, 0x42000000, v9
	ds_write2_b32 v48, v118, v119 offset1:32
	v_mov_b32_e32 v118, v3
	v_mov_b32_e32 v119, v3
	v_cvt_pk_fp8_f32 v118, v75, v74
	v_cvt_pk_fp8_f32 v119, v71, v69
	v_mul_f32_e32 v113, 0x42000000, v5
	v_mul_f32_e32 v110, 0x42000000, v17
	v_cvt_pk_fp8_f32 v118, v70, v68 op_sel:[0,0,1]
	v_cvt_pk_fp8_f32 v119, v67, v66 op_sel:[0,0,1]
	v_mul_f32_e32 v111, 0x42000000, v13
	v_mul_f32_e32 v108, 0x42000000, v10
	v_mul_f32_e32 v109, 0x42000000, v6
	ds_write2_b32 v48, v118, v119 offset0:64 offset1:96
	v_mov_b32_e32 v118, v3
	v_mov_b32_e32 v119, v3
	v_cvt_pk_fp8_f32 v118, v65, v64
	v_cvt_pk_fp8_f32 v119, v62, v61
	v_mul_f32_e32 v106, 0x42000000, v18
	v_mul_f32_e32 v107, 0x42000000, v14
	v_cvt_pk_fp8_f32 v118, v60, v59 op_sel:[0,0,1]
	v_cvt_pk_fp8_f32 v119, v56, v55 op_sel:[0,0,1]
	v_mul_f32_e32 v104, 0x42000000, v11
	v_mul_f32_e32 v105, 0x42000000, v7
	v_mul_f32_e32 v102, 0x42000000, v19
	ds_write2_b32 v63, v118, v119 offset1:32
	v_mov_b32_e32 v118, v3
	v_mov_b32_e32 v119, v3
	v_cvt_pk_fp8_f32 v118, v58, v57
	v_cvt_pk_fp8_f32 v119, v54, v52
	v_mul_f32_e32 v103, 0x42000000, v15
	v_mul_f32_e32 v100, 0x42000000, v24
	v_cvt_pk_fp8_f32 v118, v53, v51 op_sel:[0,0,1]
	v_cvt_pk_fp8_f32 v119, v50, v49 op_sel:[0,0,1]
	v_mul_f32_e32 v101, 0x42000000, v20
	v_mul_f32_e32 v98, 0x42000000, v32
	v_mul_f32_e32 v99, 0x42000000, v28
	ds_write2_b32 v63, v118, v119 offset0:64 offset1:96
	v_mov_b32_e32 v118, v3
	v_cvt_pk_fp8_f32 v118, v117, v116
	v_mul_f32_e32 v96, 0x42000000, v25
	v_mul_f32_e32 v97, 0x42000000, v21
	v_mul_f32_e32 v94, 0x42000000, v33
	v_cvt_pk_fp8_f32 v118, v115, v114 op_sel:[0,0,1]
	v_mov_b32_e32 v114, v3
	v_cvt_pk_fp8_f32 v114, v113, v112
	v_mul_f32_e32 v95, 0x42000000, v29
	v_mul_f32_e32 v92, 0x42000000, v26
	v_mul_f32_e32 v93, 0x42000000, v22
	v_cvt_pk_fp8_f32 v114, v111, v110 op_sel:[0,0,1]
	v_mov_b32_e32 v110, v3
	v_cvt_pk_fp8_f32 v110, v109, v108
	s_lshl_b64 s[2:3], s[12:13], 20
	s_add_u32 s2, s56, s2
	v_lshlrev_b32_e32 v40, 4, v82
	v_cvt_pk_fp8_f32 v110, v107, v106 op_sel:[0,0,1]
	v_mov_b32_e32 v106, v3
	v_cvt_pk_fp8_f32 v106, v105, v104
	v_mul_f32_e32 v88, 0x42000000, v34
	v_mul_f32_e32 v89, 0x42000000, v30
	s_addc_u32 s3, s57, s3
	v_cvt_pk_fp8_f32 v106, v103, v102 op_sel:[0,0,1]
	v_mov_b32_e32 v102, v3
	v_cvt_pk_fp8_f32 v102, v101, v100
	v_and_b32_e32 v40, 0x70, v40
	v_mul_f32_e32 v86, 0x42000000, v27
	v_mul_f32_e32 v87, 0x42000000, v23
	v_cvt_pk_fp8_f32 v102, v99, v98 op_sel:[0,0,1]
	v_mov_b32_e32 v98, v3
	v_cvt_pk_fp8_f32 v98, v97, v96
	s_add_u32 s2, s2, s33
	v_add_u32_e32 v84, 0xfffff800, v36
	v_add_u32_e32 v38, 0xfffff8c0, v36
	v_cvt_pk_fp8_f32 v98, v95, v94 op_sel:[0,0,1]
	v_mov_b32_e32 v94, v3
	v_cvt_pk_fp8_f32 v94, v93, v92
	v_add3_u32 v83, 0, v37, v40
	v_add_u32_e32 v40, 0xfffff880, v36
	v_add_u32_e32 v42, 0xfffff840, v36
	v_cvt_pk_fp8_f32 v94, v89, v88 op_sel:[0,0,1]
	v_mov_b32_e32 v88, v3
	v_cvt_pk_fp8_f32 v88, v87, v86
	s_addc_u32 s3, s3, 0
	v_ashrrev_i32_e32 v39, 31, v38
	v_ashrrev_i32_e32 v41, 31, v40
	v_ashrrev_i32_e32 v43, 31, v42
	v_ashrrev_i32_e32 v85, 31, v84
	v_lshl_add_u64 v[44:45], s[2:3], 0, v[2:3]
	v_lshlrev_b64 v[38:39], 10, v[38:39]
	v_lshlrev_b64 v[40:41], 10, v[40:41]
	v_lshlrev_b64 v[42:43], 10, v[42:43]
	v_lshlrev_b64 v[84:85], 10, v[84:85]
	v_lshl_add_u64 v[38:39], v[44:45], 0, v[38:39]
	v_lshl_add_u64 v[40:41], v[44:45], 0, v[40:41]
	v_lshl_add_u64 v[42:43], v[44:45], 0, v[42:43]
	v_lshl_add_u64 v[44:45], v[44:45], 0, v[84:85]
	v_mul_f32_e32 v84, 0x42000000, v35
	v_mul_f32_e32 v85, 0x42000000, v31
	v_cvt_pk_fp8_f32 v88, v85, v84 op_sel:[0,0,1]
	ds_write2_b32 v47, v118, v114 offset1:32
	ds_write2_b32 v47, v110, v106 offset0:64 offset1:96
	ds_write2_b32 v46, v102, v98 offset1:32
	ds_write2_b32 v46, v94, v88 offset0:64 offset1:96
	s_waitcnt lgkmcnt(0)
	s_barrier
	ds_read_b128 v[84:87], v83
	s_mov_b64 s[14:15], 0
	s_waitcnt lgkmcnt(0)
	global_store_dwordx4 v[44:45], v[84:87], off
	ds_read_b128 v[84:87], v83 offset:8192
	s_waitcnt lgkmcnt(0)
	global_store_dwordx4 v[42:43], v[84:87], off
	ds_read_b128 v[42:45], v83 offset:16384
	s_waitcnt lgkmcnt(0)
	global_store_dwordx4 v[40:41], v[42:45], off
	ds_read_b128 v[40:43], v83 offset:24576
	s_waitcnt lgkmcnt(0)
	global_store_dwordx4 v[38:39], v[40:43], off
	s_barrier

.LBB0_757:
	v_mov_b32_e32 v2, v0
	v_mov_b32_e32 v90, 0
	v_cmp_eq_u32_e32 vcc, 0, v2
	v_mov_b32_e32 v91, 0xc00
	s_and_saveexec_b64 s[0:1], vcc
	s_cbranch_execz .LBB0_763
	v_mov_b32_e32 v122, 1
	v_mov_b32_e32 v123, 1
	global_atomic_add v122, v3, v122, s[4:5] sc0
	global_atomic_add v123, v3, v123, s[6:7] sc0
.LBB0_763:
	s_or_b64 exec, exec, s[0:1]
	s_cmpk_gt_i32 s12, 0xbff
	s_cbranch_scc1 .Lpf_swa_skip
	s_mul_hi_i32 s84, s12, 0x2aaaaaab
	s_lshr_b32 s84, s84, 4
	s_mul_i32 s85, s84, 0xffffffa0
	s_add_i32 s85, s85, s12
	v_readlane_b32 s87, v254, 7
	v_readlane_b32 s88, v253, 1
	v_readlane_b32 s89, v253, 2
	s_lshl_b32 s86, s12, 7
	s_and_b32 s86, s86, 0x380
	v_ashrrev_i32_e32 v238, 2, v0
	v_and_b32_e32 v238, -4, v238
	v_add_u32_e32 v238, s86, v238
	v_lshlrev_b32_e32 v240, 4, v0
	v_and_b32_e32 v240, 0xf0, v240
	s_lshl_b32 s87, s87, 5
	s_add_i32 s92, s84, s87
	s_mov_b32 s93, 0
	s_cmp_gt_i32 s85, 63
	s_cbranch_scc1 .Lpf_swa_w2
	s_load_dwordx2 s[90:91], s[88:89], 0xa0
	s_lshl_b64 s[92:93], s[92:93], 23
	v_lshlrev_b32_e32 v238, 13, v238
	s_lshl_b32 s86, s85, 4
	s_and_b32 s86, s86, 0xffffff80
	s_lshl_b32 s86, s86, 2
	v_add3_u32 v238, v238, v240, s86
	v_mov_b32_e32 v239, 0
	s_waitcnt lgkmcnt(0)
	s_add_u32 s90, s90, s92
	s_addc_u32 s91, s91, s93
	v_lshl_add_u64 v[238:239], s[90:91], 0, v[238:239]
	s_mov_b64 s[94:95], 0x2000
	v_lshl_add_u64 v[240:241], v[238:239], 0, s[94:95]
	global_load_dwordx4 v[126:129], v[240:241], off nt
	s_mov_b64 s[94:95], 0x4000
	v_lshl_add_u64 v[242:243], v[238:239], 0, s[94:95]
	global_load_dwordx4 v[130:133], v[242:243], off nt
	global_load_dwordx4 v[134:137], v[238:239], off nt
	global_load_dwordx4 v[138:141], v[238:239], off offset:256 nt
	s_mov_b64 s[94:95], 0x6000
	v_lshl_add_u64 v[240:241], v[238:239], 0, s[94:95]
	global_load_dwordx4 v[142:145], v[240:241], off nt
	s_mov_b64 s[94:95], 0x2000
	v_lshl_add_u64 v[242:243], v[238:239], 0, s[94:95]
	global_load_dwordx4 v[146:149], v[242:243], off offset:256 nt
	s_mov_b64 s[94:95], 0x4000
	v_lshl_add_u64 v[240:241], v[238:239], 0, s[94:95]
	global_load_dwordx4 v[168:171], v[240:241], off offset:256 nt
	s_mov_b64 s[94:95], 0x6000
	v_lshl_add_u64 v[242:243], v[238:239], 0, s[94:95]
	global_load_dwordx4 v[172:175], v[242:243], off offset:256 nt
	s_mov_b64 s[94:95], 0x1000
	v_lshl_add_u64 v[240:241], v[238:239], 0, s[94:95]
	global_load_dwordx4 v[176:179], v[240:241], off nt
	s_mov_b64 s[94:95], 0x3000
	v_lshl_add_u64 v[242:243], v[238:239], 0, s[94:95]
	global_load_dwordx4 v[206:209], v[242:243], off nt
	s_mov_b64 s[94:95], 0x5000
	v_lshl_add_u64 v[240:241], v[238:239], 0, s[94:95]
	global_load_dwordx4 v[210:213], v[240:241], off nt
	s_mov_b64 s[94:95], 0x7000
	v_lshl_add_u64 v[242:243], v[238:239], 0, s[94:95]
	global_load_dwordx4 v[214:217], v[242:243], off nt
	s_mov_b64 s[94:95], 0x1000
	v_lshl_add_u64 v[240:241], v[238:239], 0, s[94:95]
	global_load_dwordx4 v[222:225], v[240:241], off offset:256 nt
	s_mov_b64 s[94:95], 0x3000
	v_lshl_add_u64 v[242:243], v[238:239], 0, s[94:95]
	global_load_dwordx4 v[226:229], v[242:243], off offset:256 nt
	s_mov_b64 s[94:95], 0x5000
	v_lshl_add_u64 v[240:241], v[238:239], 0, s[94:95]
	global_load_dwordx4 v[230:233], v[240:241], off offset:256 nt
	s_mov_b64 s[94:95], 0x7000
	v_lshl_add_u64 v[242:243], v[238:239], 0, s[94:95]
	global_load_dwordx4 v[234:237], v[242:243], off offset:256 nt
	s_branch .Lpf_swa_skip

.Lpf_swa_skip:
	v_mov_b32_e32 v4, v0
	s_nop 0
	v_readfirstlane_b32 s15, v4
	s_ashr_i32 s14, s15, 6
	s_cmp_lt_i32 s14, 4
	s_cbranch_scc1 .LBB0_765
	s_setprio 1

.LBB0_768:
	s_and_b32 s14, s14, 3
	s_lshl_b32 s17, s17, 2
	s_or_b32 s14, s14, s17
	s_add_i32 s17, s14, 1
	v_cvt_f32_ubyte0_e32 v2, s17
	s_mov_b32 s17, 0x42fc0000
	v_cmp_lt_f32_e32 vcc, s17, v2
	v_mov_b32_e32 v5, 0x42800000
	s_ashr_i32 s15, s15, 3
	v_cndmask_b32_e32 v5, 0, v5, vcc
	s_andn2_b32 s15, s15, 31
	v_sub_f32_e32 v2, v5, v2
	v_and_b32_e32 v102, 31, v4
	s_add_i32 s16, s15, s16
	v_exp_f32_e32 v2, v2
	v_or_b32_e32 v94, s16, v102
	s_and_b64 s[18:19], vcc, exec
	v_ashrrev_i32_e32 v95, 31, v94
	s_cselect_b32 s18, 0xffffffc0, 0
	v_lshl_add_u64 v[92:93], v[94:95], 0, s[82:83]
	v_mov_b64_e32 v[6:7], s[50:51]
	v_ldexp_f32 v100, v2, s18
	v_mad_u64_u32 v[6:7], s[18:19], v92, s70, v[6:7]
	v_bfe_u32 v101, v4, 5, 1
	v_mad_i32_i24 v7, v93, s70, v7
	s_lshl_b32 s82, s14, 7
	v_lshl_add_u64 v[6:7], v[6:7], 0, s[82:83]
	v_lshlrev_b32_e32 v2, 4, v101
	v_lshl_add_u64 v[6:7], v[6:7], 0, v[2:3]
	global_load_dwordx4 v[66:69], v[6:7], off
	global_load_dwordx4 v[70:73], v[6:7], off offset:32
	global_load_dwordx4 v[74:77], v[6:7], off offset:64
	global_load_dwordx4 v[78:81], v[6:7], off offset:96
	s_load_dwordx2 s[18:19], s[48:49], 0x40
	s_or_b32 s82, s14, s33
	s_lshl_b64 s[20:21], s[82:83], 2
	s_mov_b32 s17, 0
	s_waitcnt lgkmcnt(0)
	s_add_u32 s18, s18, s20
	s_addc_u32 s19, s19, s21
	global_load_dword v95, v3, s[18:19]
	s_cmp_lt_i32 s13, 0
	s_waitcnt vmcnt(0)
	v_mov_b32_e32 v90, v122
	v_min_u32_e32 v91, 0xc00, v123
	.p2align 8
	s_cbranch_scc1 .LBB0_793
	v_and_b32_e32 v2, 63, v4
	v_mul_f32_e32 v4, 0x43800000, v100
	v_and_b32_e32 v5, 0x7fff0000, v100
	v_or_b32_sdwa v4, v4, v5 dst_sel:DWORD dst_unused:UNUSED_PAD src0_sel:WORD_1 src1_sel:DWORD
	v_lshlrev_b32_e32 v5, 7, v2
	v_and_b32_e32 v103, 0xf00, v5
	v_lshlrev_b32_e32 v5, 3, v2
	v_and_b32_e32 v96, 8, v5
	v_bfe_u32 v6, v2, 1, 4
	v_or_b32_e32 v5, v96, v101
	v_bitop3_b32 v7, v96, v6, v101 bitop3:0x36
	v_lshlrev_b32_e32 v104, 4, v7
	v_bitop3_b32 v7, v5, v6, 2 bitop3:0x36
	v_lshlrev_b32_e32 v105, 4, v7
	v_bitop3_b32 v7, v5, v6, 4 bitop3:0x36
	v_bitop3_b32 v5, v5, v6, 6 bitop3:0x36
	v_lshlrev_b32_e32 v107, 4, v5
	v_lshrrev_b32_e32 v5, 2, v2
	v_cmp_gt_u32_e64 s[36:37], 32, v2
	v_lshlrev_b32_e32 v106, 4, v7
	v_and_b32_e32 v5, 2, v5
	v_lshrrev_b32_e32 v6, 3, v2
	v_bfe_u32 v7, v2, 1, 1
	v_cndmask_b32_e64 v82, 0, v4, s[36:37]
	v_lshrrev_b32_e32 v4, 1, v2
	v_and_or_b32 v5, v6, 4, v5
	v_and_or_b32 v6, v6, 2, v7
	v_bfe_u32 v2, v2, 3, 1
	v_and_or_b32 v2, v4, 2, v2
	v_lshlrev_b32_e32 v4, 4, v6
	v_lshl_or_b32 v2, v2, 6, v4
	v_lshlrev_b32_e32 v4, 2, v101
	v_lshlrev_b32_e32 v5, 7, v5
	v_or_b32_e32 v109, v2, v5
	v_bitop3_b32 v110, v2, 64, v5 bitop3:0x36
	v_sub_u32_e32 v2, v4, v102
	v_mov_b32_e32 v16, v3
	v_mov_b32_e32 v17, v3
	s_add_i32 s22, s0, s1
	s_sub_i32 s23, 0, s0
	s_lshl_b32 s0, s0, 6
	v_sub_u32_e32 v111, v102, v4
	v_subrev_u32_e32 v112, s15, v2
	v_mov_b32_e32 v2, v3
	v_mov_b32_e32 v4, v3
	v_mov_b32_e32 v5, v3
	v_mov_b32_e32 v6, v3
	v_mov_b32_e32 v7, v3
	v_mov_b32_e32 v8, v3
	v_mov_b32_e32 v9, v3
	v_mov_b32_e32 v10, v3
	v_mov_b32_e32 v11, v3
	v_mov_b32_e32 v12, v3
	v_mov_b32_e32 v13, v3
	v_mov_b32_e32 v14, v3
	v_mov_b32_e32 v15, v3
	v_mov_b64_e32 v[32:33], v[16:17]
	v_mov_b64_e32 v[48:49], v[16:17]
	s_mov_b32 s18, 32
	v_mov_b32_e32 v83, v3
	v_mov_b32_e32 v84, v3
	v_mov_b32_e32 v85, v3
	s_or_b32 s19, s16, 31
	s_add_i32 s20, s16, 0xffffff81
	s_mov_b32 s21, 3
	s_sub_i32 s22, 0, s22
	s_sub_i32 s24, s23, s1
	s_sub_i32 s25, 0, s0
	v_mov_b32_e32 v113, 0xf149f2ca
	v_mov_b32_e32 v108, 0
	s_mov_b32 s26, 0
	v_mov_b64_e32 v[30:31], v[14:15]
	v_mov_b64_e32 v[28:29], v[12:13]
	v_mov_b64_e32 v[26:27], v[10:11]
	v_mov_b64_e32 v[24:25], v[8:9]
	v_mov_b64_e32 v[22:23], v[6:7]
	v_mov_b64_e32 v[20:21], v[4:5]
	v_mov_b64_e32 v[18:19], v[2:3]
	v_mov_b64_e32 v[46:47], v[14:15]
	v_mov_b64_e32 v[44:45], v[12:13]
	v_mov_b64_e32 v[42:43], v[10:11]
	v_mov_b64_e32 v[40:41], v[8:9]
	v_mov_b64_e32 v[38:39], v[6:7]
	v_mov_b64_e32 v[36:37], v[4:5]
	v_mov_b64_e32 v[34:35], v[2:3]
	s_branch .LBB0_772

.LBB0_800:
	v_lshlrev_b32_e32 v36, 4, v38
	v_and_b32_e32 v2, 0xf0, v36
	v_lshl_add_u64 v[28:29], v[4:5], 0, v[2:3]
	v_lshl_add_u64 v[4:5], v[28:29], 0, s[38:39]
	v_lshl_add_u64 v[6:7], v[28:29], 0, s[36:37]
	v_mov_b32_e32 v40, v126
	v_mov_b32_e32 v41, v127
	v_mov_b32_e32 v42, v128
	v_mov_b32_e32 v43, v129
	v_mov_b32_e32 v44, v130
	v_mov_b32_e32 v45, v131
	v_mov_b32_e32 v46, v132
	v_mov_b32_e32 v47, v133
	v_lshl_add_u64 v[4:5], v[28:29], 0, s[34:35]
	v_mov_b32_e32 v84, v134
	v_mov_b32_e32 v85, v135
	v_mov_b32_e32 v86, v136
	v_mov_b32_e32 v87, v137
	v_mov_b32_e32 v66, v138
	v_mov_b32_e32 v67, v139
	v_mov_b32_e32 v68, v140
	v_mov_b32_e32 v69, v141
	v_lshl_add_u64 v[6:7], v[28:29], 0, s[30:31]
	v_mov_b32_e32 v76, v142
	v_mov_b32_e32 v77, v143
	v_mov_b32_e32 v78, v144
	v_mov_b32_e32 v79, v145
	v_mov_b32_e32 v70, v146
	v_mov_b32_e32 v71, v147
	v_mov_b32_e32 v72, v148
	v_mov_b32_e32 v73, v149
	v_lshl_add_u64 v[4:5], v[28:29], 0, s[28:29]
	v_lshl_add_u64 v[6:7], v[28:29], 0, s[26:27]
	v_mov_b32_e32 v60, v168
	v_mov_b32_e32 v61, v169
	v_mov_b32_e32 v62, v170
	v_mov_b32_e32 v63, v171
	v_mov_b32_e32 v92, v172
	v_mov_b32_e32 v93, v173
	v_mov_b32_e32 v94, v174
	v_mov_b32_e32 v95, v175
	v_lshl_add_u64 v[4:5], v[28:29], 0, s[24:25]
	v_lshl_add_u64 v[8:9], v[28:29], 0, s[22:23]
	v_lshl_add_u64 v[12:13], v[28:29], 0, s[20:21]
	v_lshl_add_u64 v[16:17], v[28:29], 0, s[18:19]
	v_lshl_add_u64 v[20:21], v[28:29], 0, s[16:17]
	v_lshl_add_u64 v[24:25], v[28:29], 0, s[14:15]
	v_lshl_add_u64 v[30:31], v[28:29], 0, s[12:13]
	v_lshl_add_u64 v[32:33], v[28:29], 0, s[2:3]
	v_mov_b32_e32 v4, v176
	v_mov_b32_e32 v5, v177
	v_mov_b32_e32 v6, v178
	v_mov_b32_e32 v7, v179
	v_mov_b32_e32 v8, v206
	v_mov_b32_e32 v9, v207
	v_mov_b32_e32 v10, v208
	v_mov_b32_e32 v11, v209
	v_mov_b32_e32 v12, v210
	v_mov_b32_e32 v13, v211
	v_mov_b32_e32 v14, v212
	v_mov_b32_e32 v15, v213
	v_mov_b32_e32 v16, v214
	v_mov_b32_e32 v17, v215
	v_mov_b32_e32 v18, v216
	v_mov_b32_e32 v19, v217
	v_mov_b32_e32 v20, v222
	v_mov_b32_e32 v21, v223
	v_mov_b32_e32 v22, v224
	v_mov_b32_e32 v23, v225
	v_mov_b32_e32 v24, v226
	v_mov_b32_e32 v25, v227
	v_mov_b32_e32 v26, v228
	v_mov_b32_e32 v27, v229
	v_mov_b32_e32 v28, v230
	v_mov_b32_e32 v29, v231
	v_mov_b32_e32 v30, v232
	v_mov_b32_e32 v31, v233
	v_mov_b32_e32 v32, v234
	v_mov_b32_e32 v33, v235
	v_mov_b32_e32 v34, v236
	v_mov_b32_e32 v35, v237
	v_ashrrev_i32_e32 v39, 6, v38
	v_lshlrev_b32_e32 v37, 9, v38
	v_bitop3_b32 v39, v39, v38, 7 bitop3:0x78
	v_lshrrev_b32_e32 v2, 2, v38
	v_and_b32_e32 v37, 0x1e00, v37
	v_lshlrev_b32_e32 v39, 4, v39
	v_add3_u32 v39, 0, v37, v39
	v_and_b32_e32 v48, 12, v2
	v_ashrrev_i32_e32 v37, 3, v38
	v_lshrrev_b32_e32 v49, 5, v38
	v_add_u32_e32 v48, v39, v48
	v_and_b32_e32 v2, 0x70, v36
	v_add_u32_e32 v36, s46, v37
	s_mov_b64 s[2:3], -1
	s_and_b64 vcc, exec, s[0:1]
	v_lshlrev_b32_e32 v37, 7, v37
	v_xor_b32_e32 v82, v49, v38
	v_mul_f32_e32 v49, 0x42000000, v95
	v_mul_f32_e32 v50, 0x42000000, v63
	v_mul_f32_e32 v52, 0x42000000, v73
	v_mul_f32_e32 v54, 0x42000000, v69
	v_mul_f32_e32 v51, 0x42000000, v94
	v_mul_f32_e32 v53, 0x42000000, v62
	v_mul_f32_e32 v57, 0x42000000, v72
	v_mul_f32_e32 v58, 0x42000000, v68
	v_mul_f32_e32 v55, 0x42000000, v93
	v_mul_f32_e32 v56, 0x42000000, v61
	v_mul_f32_e32 v61, 0x42000000, v71
	v_mul_f32_e32 v62, 0x42000000, v67
	v_mul_f32_e32 v59, 0x42000000, v92
	v_mul_f32_e32 v60, 0x42000000, v60
	v_mul_f32_e32 v64, 0x42000000, v70
	v_mul_f32_e32 v65, 0x42000000, v66
	v_mul_f32_e32 v66, 0x42000000, v79
	v_mul_f32_e32 v67, 0x42000000, v47
	v_mul_f32_e32 v69, 0x42000000, v43
	v_mul_f32_e32 v71, 0x42000000, v87
	v_mul_f32_e32 v68, 0x42000000, v78
	v_mul_f32_e32 v70, 0x42000000, v46
	v_mul_f32_e32 v74, 0x42000000, v42
	v_mul_f32_e32 v75, 0x42000000, v86
	v_mul_f32_e32 v72, 0x42000000, v77
	v_mul_f32_e32 v73, 0x42000000, v45
	v_mul_f32_e32 v78, 0x42000000, v41
	v_mul_f32_e32 v79, 0x42000000, v85
	v_mul_f32_e32 v76, 0x42000000, v76
	v_mul_f32_e32 v77, 0x42000000, v44
	v_mul_f32_e32 v80, 0x42000000, v40
	v_mul_f32_e32 v81, 0x42000000, v84
	v_add_u32_e32 v63, 0x2000, v48
	v_add_u32_e32 v47, 0x4000, v48
	v_add_u32_e32 v46, 0x6000, v48
	s_barrier
	s_cbranch_vccz .LBB0_802
	v_mov_b32_e32 v118, v3
	v_mov_b32_e32 v119, v3
	v_cvt_pk_fp8_f32 v118, v81, v80
	v_cvt_pk_fp8_f32 v119, v79, v78
	v_mul_f32_e32 v116, 0x42000000, v8
	v_mul_f32_e32 v117, 0x42000000, v4
	v_cvt_pk_fp8_f32 v118, v77, v76 op_sel:[0,0,1]
	v_cvt_pk_fp8_f32 v119, v73, v72 op_sel:[0,0,1]
	v_mul_f32_e32 v114, 0x42000000, v16
	v_mul_f32_e32 v115, 0x42000000, v12
	v_mul_f32_e32 v112, 0x42000000, v9
	ds_write2_b32 v48, v118, v119 offset1:32
	v_mov_b32_e32 v118, v3
	v_mov_b32_e32 v119, v3
	v_cvt_pk_fp8_f32 v118, v75, v74
	v_cvt_pk_fp8_f32 v119, v71, v69
	v_mul_f32_e32 v113, 0x42000000, v5
	v_mul_f32_e32 v110, 0x42000000, v17
	v_cvt_pk_fp8_f32 v118, v70, v68 op_sel:[0,0,1]
	v_cvt_pk_fp8_f32 v119, v67, v66 op_sel:[0,0,1]
	v_mul_f32_e32 v111, 0x42000000, v13
	v_mul_f32_e32 v108, 0x42000000, v10
	v_mul_f32_e32 v109, 0x42000000, v6
	ds_write2_b32 v48, v118, v119 offset0:64 offset1:96
	v_mov_b32_e32 v118, v3
	v_mov_b32_e32 v119, v3
	v_cvt_pk_fp8_f32 v118, v65, v64
	v_cvt_pk_fp8_f32 v119, v62, v61
	v_mul_f32_e32 v106, 0x42000000, v18
	v_mul_f32_e32 v107, 0x42000000, v14
	v_cvt_pk_fp8_f32 v118, v60, v59 op_sel:[0,0,1]
	v_cvt_pk_fp8_f32 v119, v56, v55 op_sel:[0,0,1]
	v_mul_f32_e32 v104, 0x42000000, v11
	v_mul_f32_e32 v105, 0x42000000, v7
	v_mul_f32_e32 v102, 0x42000000, v19
	ds_write2_b32 v63, v118, v119 offset1:32
	v_mov_b32_e32 v118, v3
	v_mov_b32_e32 v119, v3
	v_cvt_pk_fp8_f32 v118, v58, v57
	v_cvt_pk_fp8_f32 v119, v54, v52
	v_mul_f32_e32 v103, 0x42000000, v15
	v_mul_f32_e32 v100, 0x42000000, v24
	v_cvt_pk_fp8_f32 v118, v53, v51 op_sel:[0,0,1]
	v_cvt_pk_fp8_f32 v119, v50, v49 op_sel:[0,0,1]
	v_mul_f32_e32 v101, 0x42000000, v20
	v_mul_f32_e32 v98, 0x42000000, v32
	v_mul_f32_e32 v99, 0x42000000, v28
	ds_write2_b32 v63, v118, v119 offset0:64 offset1:96
	v_mov_b32_e32 v118, v3
	v_cvt_pk_fp8_f32 v118, v117, v116
	v_mul_f32_e32 v96, 0x42000000, v25
	v_mul_f32_e32 v97, 0x42000000, v21
	v_mul_f32_e32 v94, 0x42000000, v33
	v_cvt_pk_fp8_f32 v118, v115, v114 op_sel:[0,0,1]
	v_mov_b32_e32 v114, v3
	v_cvt_pk_fp8_f32 v114, v113, v112
	v_mul_f32_e32 v95, 0x42000000, v29
	v_mul_f32_e32 v92, 0x42000000, v26
	v_mul_f32_e32 v93, 0x42000000, v22
	v_cvt_pk_fp8_f32 v114, v111, v110 op_sel:[0,0,1]
	v_mov_b32_e32 v110, v3
	v_cvt_pk_fp8_f32 v110, v109, v108
	s_lshl_b64 s[0:1], s[10:11], 20
	s_add_u32 s0, s41, s0
	v_lshlrev_b32_e32 v40, 4, v82
	v_cvt_pk_fp8_f32 v110, v107, v106 op_sel:[0,0,1]
	v_mov_b32_e32 v106, v3
	v_cvt_pk_fp8_f32 v106, v105, v104
	v_mul_f32_e32 v88, 0x42000000, v34
	v_mul_f32_e32 v89, 0x42000000, v30
	s_addc_u32 s1, s42, s1
	v_cvt_pk_fp8_f32 v106, v103, v102 op_sel:[0,0,1]
	v_mov_b32_e32 v102, v3
	v_cvt_pk_fp8_f32 v102, v101, v100
	v_and_b32_e32 v40, 0x70, v40
	v_mul_f32_e32 v86, 0x42000000, v27
	v_mul_f32_e32 v87, 0x42000000, v23
	v_cvt_pk_fp8_f32 v102, v99, v98 op_sel:[0,0,1]
	v_mov_b32_e32 v98, v3
	v_cvt_pk_fp8_f32 v98, v97, v96
	s_add_u32 s0, s0, s45
	v_add_u32_e32 v84, 0xfffff800, v36
	v_add_u32_e32 v38, 0xfffff8c0, v36
	v_cvt_pk_fp8_f32 v98, v95, v94 op_sel:[0,0,1]
	v_mov_b32_e32 v94, v3
	v_cvt_pk_fp8_f32 v94, v93, v92
	v_add3_u32 v83, 0, v37, v40
	v_add_u32_e32 v40, 0xfffff880, v36
	v_add_u32_e32 v42, 0xfffff840, v36
	v_cvt_pk_fp8_f32 v94, v89, v88 op_sel:[0,0,1]
	v_mov_b32_e32 v88, v3
	v_cvt_pk_fp8_f32 v88, v87, v86
	s_addc_u32 s1, s1, 0
	v_ashrrev_i32_e32 v39, 31, v38
	v_ashrrev_i32_e32 v41, 31, v40
	v_ashrrev_i32_e32 v43, 31, v42
	v_ashrrev_i32_e32 v85, 31, v84
	v_lshl_add_u64 v[44:45], s[0:1], 0, v[2:3]
	v_lshlrev_b64 v[38:39], 10, v[38:39]
	v_lshlrev_b64 v[40:41], 10, v[40:41]
	v_lshlrev_b64 v[42:43], 10, v[42:43]
	v_lshlrev_b64 v[84:85], 10, v[84:85]
	v_lshl_add_u64 v[38:39], v[44:45], 0, v[38:39]
	v_lshl_add_u64 v[40:41], v[44:45], 0, v[40:41]
	v_lshl_add_u64 v[42:43], v[44:45], 0, v[42:43]
	v_lshl_add_u64 v[44:45], v[44:45], 0, v[84:85]
	v_mul_f32_e32 v84, 0x42000000, v35
	v_mul_f32_e32 v85, 0x42000000, v31
	v_cvt_pk_fp8_f32 v88, v85, v84 op_sel:[0,0,1]
	ds_write2_b32 v47, v118, v114 offset1:32
	ds_write2_b32 v47, v110, v106 offset0:64 offset1:96
	ds_write2_b32 v46, v102, v98 offset1:32
	ds_write2_b32 v46, v94, v88 offset0:64 offset1:96
	s_waitcnt lgkmcnt(0)
	s_barrier
	ds_read_b128 v[84:87], v83
	s_mov_b64 s[2:3], 0
	s_waitcnt lgkmcnt(0)
	global_store_dwordx4 v[44:45], v[84:87], off
	ds_read_b128 v[84:87], v83 offset:8192
	s_waitcnt lgkmcnt(0)
	global_store_dwordx4 v[42:43], v[84:87], off
	ds_read_b128 v[42:45], v83 offset:16384
	s_waitcnt lgkmcnt(0)
	global_store_dwordx4 v[40:41], v[42:45], off
	ds_read_b128 v[40:43], v83 offset:24576
	s_waitcnt lgkmcnt(0)
	global_store_dwordx4 v[38:39], v[40:43], off
	s_barrier
